# attention tile loops: K-fragment LDS reads pipelined ahead of QK^T MFMAs, LDS-DMA issue moved from softmax block into MFMA block, kmax load hoisted (no vmcnt(0) drain)
# speedup vs baseline: 1.0063x; 1.0063x over previous
.LBB0_1036:
	v_lshlrev_b32_e32 v4, 1, v119
	v_readlane_b32 s4, v254, 27
	v_lshlrev_b32_e32 v3, 4, v119
	v_and_b32_e32 v4, 32, v4
	v_lshl_add_u32 v120, v117, 2, s4
	v_lshl_add_u32 v109, v118, 4, s4
	s_movk_i32 s4, 0x118
	v_and_b32_e32 v3, 0xc0, v3
	v_and_or_b32 v2, v2, s4, v4
	v_readlane_b32 s4, v254, 35
	v_lshlrev_b32_e32 v4, 2, v118
	v_mov_b32_e32 v16, v1
	v_add3_u32 v121, v3, s4, v2
	v_add_u32_e32 v2, s0, v117
	v_mov_b32_e32 v17, v1
	v_sub_u32_e32 v122, v2, v4
	v_mov_b32_e32 v2, v1
	v_mov_b32_e32 v3, v1
	v_mov_b32_e32 v4, v1
	v_mov_b32_e32 v5, v1
	v_mov_b32_e32 v6, v1
	v_mov_b32_e32 v7, v1
	v_mov_b32_e32 v8, v1
	v_mov_b32_e32 v9, v1
	v_mov_b32_e32 v10, v1
	v_mov_b32_e32 v11, v1
	v_mov_b32_e32 v12, v1
	v_mov_b32_e32 v13, v1
	v_mov_b32_e32 v14, v1
	v_mov_b32_e32 v15, v1
	v_mov_b64_e32 v[32:33], v[16:17]
	s_add_i32 s77, s0, 31
	v_cmp_gt_u32_e64 s[10:11], 32, v119
	s_mov_b32 s86, 1
	s_add_i32 s78, s84, -1
	s_mov_b32 s80, 0
	s_sub_i32 s81, 0, s84
	v_mov_b32_e32 v123, 0
	s_mov_b32 s82, 63
	v_mov_b64_e32 v[30:31], v[14:15]
	v_mov_b64_e32 v[28:29], v[12:13]
	v_mov_b64_e32 v[26:27], v[10:11]
	v_mov_b64_e32 v[24:25], v[8:9]
	v_mov_b64_e32 v[22:23], v[6:7]
	v_mov_b64_e32 v[20:21], v[4:5]
	v_mov_b64_e32 v[18:19], v[2:3]
	v_mov_b32_e32 v124, 0
	s_add_i32 s14, s86, 2
	s_min_i32 s4, s14, s78
	s_ashr_i32 s5, s4, 31
	s_lshl_b64 s[12:13], s[4:5], 16
	s_and_b32 s5, s14, 3
	s_mulk_i32 s5, 0x3000
	v_lshl_add_u64 v[196:197], v[110:111], 0, s[12:13]
	s_add_i32 s12, s5, s85
	s_mov_b32 s13, m0
	s_mov_b32 m0, s12
	s_nop 0
	global_load_lds_dwordx4 v[196:197], off
	s_mov_b32 m0, s13
	s_and_b64 vcc, exec, s[8:9]
	s_cbranch_vccnz .Lmla_dma_v2
	v_mad_i64_i32 v[196:197], s[12:13], s4, v235, v[112:113]
	v_readlane_b32 s4, v254, 28
	s_add_i32 s4, s5, s4
	s_mov_b32 s5, m0
	s_mov_b32 m0, s4
	s_nop 0
	global_load_lds_dwordx4 v[196:197], off
	s_mov_b32 m0, s5
.Lmla_dma_v2:
	s_add_i32 s12, s86, 1
	s_min_i32 s12, s12, s78
	s_ashr_i32 s13, s12, 31
	s_add_i32 s15, s80, 0x4000
	s_lshl_b64 s[12:13], s[12:13], 16
	s_and_b32 s15, s15, 0x6000
	v_readlane_b32 s16, v254, 34
	s_add_i32 s15, s15, s16
	v_lshl_add_u64 v[196:197], v[114:115], 0, s[12:13]
	s_mov_b32 s12, m0
	s_mov_b32 m0, s15
	s_nop 0
	global_load_lds_dwordx4 v[196:197], off
	s_mov_b32 m0, s12
.LBB0_1037:
	s_sub_i32 s14, s82, 63
	s_cmp_le_i32 s14, s77
	s_cselect_b64 s[4:5], -1, 0
	s_add_i32 s83, s86, 1
	s_cmp_gt_i32 s14, s77
	s_cbranch_scc1 .LBB0_1045
	v_sub_f32_e32 v65, v65, v123
	v_sub_f32_e32 v64, v64, v123
	v_sub_f32_e32 v63, v63, v123
	v_sub_f32_e32 v62, v62, v123
	v_sub_f32_e32 v61, v61, v123
	v_sub_f32_e32 v60, v60, v123
	v_sub_f32_e32 v59, v59, v123
	v_sub_f32_e32 v58, v58, v123
	v_sub_f32_e32 v57, v57, v123
	v_sub_f32_e32 v56, v56, v123
	v_sub_f32_e32 v55, v55, v123
	v_sub_f32_e32 v54, v54, v123
	v_sub_f32_e32 v53, v53, v123
	v_sub_f32_e32 v52, v52, v123
	v_sub_f32_e32 v51, v51, v123
	v_sub_f32_e32 v50, v50, v123
	v_sub_f32_e32 v49, v49, v123
	v_sub_f32_e32 v48, v48, v123
	v_sub_f32_e32 v47, v47, v123
	v_sub_f32_e32 v46, v46, v123
	v_sub_f32_e32 v45, v45, v123
	v_sub_f32_e32 v44, v44, v123
	v_sub_f32_e32 v43, v43, v123
	v_sub_f32_e32 v42, v42, v123
	v_sub_f32_e32 v41, v41, v123
	v_sub_f32_e32 v40, v40, v123
	v_sub_f32_e32 v39, v39, v123
	v_sub_f32_e32 v38, v38, v123
	v_sub_f32_e32 v37, v37, v123
	v_sub_f32_e32 v36, v36, v123
	v_sub_f32_e32 v35, v35, v123
	s_cmp_le_i32 s82, s0
	v_sub_f32_e32 v34, v34, v123
	s_cbranch_scc1 .LBB0_1042
	v_mov_b32_e32 v90, v122
	s_nop 0
	v_cmp_gt_i32_e64 s[70:71], 26, v90
	v_cmp_gt_i32_e64 s[72:73], 27, v90
	v_cmp_gt_i32_e64 s[68:69], 25, v90
	s_and_b64 s[70:71], s[72:73], s[70:71]
	v_cmp_gt_i32_e64 s[66:67], 24, v90
	s_and_b64 s[68:69], s[70:71], s[68:69]
	v_cmp_gt_i32_e64 s[64:65], 19, v90
	s_and_b64 s[66:67], s[68:69], s[66:67]
	v_cmp_gt_i32_e64 s[62:63], 18, v90
	s_and_b64 s[64:65], s[66:67], s[64:65]
	v_cmp_gt_i32_e64 s[60:61], 17, v90
	s_and_b64 s[62:63], s[64:65], s[62:63]
	v_cmp_gt_i32_e64 s[58:59], 16, v90
	s_and_b64 s[60:61], s[62:63], s[60:61]
	v_cmp_gt_i32_e64 s[56:57], 11, v90
	s_and_b64 s[58:59], s[60:61], s[58:59]
	v_cmp_gt_i32_e64 s[54:55], 10, v90
	s_and_b64 s[56:57], s[58:59], s[56:57]
	v_cmp_gt_i32_e64 s[52:53], 9, v90
	s_and_b64 s[54:55], s[56:57], s[54:55]
	v_cmp_gt_i32_e64 s[50:51], 8, v90
	s_and_b64 s[52:53], s[54:55], s[52:53]
	v_cmp_gt_i32_e64 s[48:49], 3, v90
	s_and_b64 s[50:51], s[52:53], s[50:51]
	v_cmp_gt_i32_e64 s[46:47], 2, v90
	s_and_b64 s[48:49], s[50:51], s[48:49]
	v_cmp_gt_i32_e64 s[44:45], 1, v90
	s_and_b64 s[46:47], s[48:49], s[46:47]
	v_cmp_gt_i32_e64 s[42:43], 0, v90
	s_and_b64 s[44:45], s[46:47], s[44:45]
	s_and_b64 s[42:43], s[44:45], s[42:43]
	v_cmp_gt_i32_e64 s[40:41], 58, v90
	v_cndmask_b32_e64 v50, v50, v240, s[42:43]
	v_cmp_gt_i32_e64 s[42:43], 59, v90
	v_cmp_gt_i32_e64 s[38:39], 57, v90
	s_and_b64 s[40:41], s[42:43], s[40:41]
	v_cmp_gt_i32_e64 s[36:37], 56, v90
	s_and_b64 s[38:39], s[40:41], s[38:39]
	v_cmp_gt_i32_e64 s[34:35], 51, v90
	s_and_b64 s[36:37], s[38:39], s[36:37]
	v_cmp_gt_i32_e64 s[30:31], 50, v90
	s_and_b64 s[34:35], s[36:37], s[34:35]
	v_cmp_gt_i32_e64 s[28:29], 49, v90
	s_and_b64 s[30:31], s[34:35], s[30:31]
	v_cmp_gt_i32_e64 s[26:27], 48, v90
	s_and_b64 s[28:29], s[30:31], s[28:29]
	v_cmp_gt_i32_e64 s[24:25], 43, v90
	s_and_b64 s[26:27], s[28:29], s[26:27]
	v_cmp_gt_i32_e64 s[22:23], 42, v90
	s_and_b64 s[24:25], s[26:27], s[24:25]
	v_cmp_gt_i32_e64 s[20:21], 41, v90
	s_and_b64 s[22:23], s[24:25], s[22:23]
	v_cmp_gt_i32_e64 s[18:19], 40, v90
	s_and_b64 s[20:21], s[22:23], s[20:21]
	v_cmp_gt_i32_e64 s[16:17], 35, v90
	s_and_b64 s[18:19], s[20:21], s[18:19]
	v_cmp_gt_i32_e64 s[14:15], 34, v90
	s_and_b64 s[16:17], s[18:19], s[16:17]
	v_cmp_gt_i32_e64 s[12:13], 33, v90
	s_and_b64 s[14:15], s[16:17], s[14:15]
	v_cmp_gt_i32_e32 vcc, 32, v90
	s_and_b64 s[12:13], s[14:15], s[12:13]
	s_and_b64 vcc, s[12:13], vcc
	v_cndmask_b32_e64 v65, v65, v240, s[72:73]
	v_cndmask_b32_e64 v64, v64, v240, s[70:71]
	v_cndmask_b32_e64 v63, v63, v240, s[68:69]
	v_cndmask_b32_e64 v62, v62, v240, s[66:67]
	v_cndmask_b32_e64 v61, v61, v240, s[64:65]
	s_mov_b64 s[64:65], 0x1f040080
	v_cndmask_b32_e64 v60, v60, v240, s[62:63]
	v_cndmask_b32_e64 v59, v59, v240, s[60:61]
	v_cndmask_b32_e64 v58, v58, v240, s[58:59]
	s_mov_b64 s[58:59], 0x2000
	v_cndmask_b32_e64 v57, v57, v240, s[56:57]
	v_cndmask_b32_e64 v56, v56, v240, s[54:55]
	v_cndmask_b32_e64 v55, v55, v240, s[52:53]
	v_cndmask_b32_e64 v54, v54, v240, s[50:51]
	v_cndmask_b32_e64 v53, v53, v240, s[48:49]
	v_cndmask_b32_e64 v52, v52, v240, s[46:47]
	v_cndmask_b32_e64 v51, v51, v240, s[44:45]
	v_cndmask_b32_e64 v49, v49, v240, s[42:43]
	v_cndmask_b32_e64 v48, v48, v240, s[40:41]
	v_cndmask_b32_e64 v47, v47, v240, s[38:39]
	v_cndmask_b32_e64 v46, v46, v240, s[36:37]
	v_cndmask_b32_e64 v45, v45, v240, s[34:35]
	v_cndmask_b32_e64 v44, v44, v240, s[30:31]
	v_cndmask_b32_e64 v43, v43, v240, s[28:29]
	v_cndmask_b32_e64 v42, v42, v240, s[26:27]
	v_cndmask_b32_e64 v41, v41, v240, s[24:25]
	v_cndmask_b32_e64 v40, v40, v240, s[22:23]
	v_cndmask_b32_e64 v39, v39, v240, s[20:21]
	v_cndmask_b32_e64 v38, v38, v240, s[18:19]
	v_cndmask_b32_e64 v37, v37, v240, s[16:17]
	v_cndmask_b32_e64 v36, v36, v240, s[14:15]
	v_cndmask_b32_e64 v35, v35, v240, s[12:13]
	v_cndmask_b32_e32 v34, v34, v240, vcc

.LBB0_1048:
	s_and_b32 s4, s80, 0x6000
	v_add_u32_e32 v125, s4, v121
	s_and_b32 s4, s86, 3
	s_mulk_i32 s4, 0x3000
	v_add_u32_e32 v142, s4, v107
	ds_read_b64_tr_b16 v[126:127], v125 offset:0
	ds_read_b64_tr_b16 v[128:129], v125 offset:0x400
	ds_read_b64_tr_b16 v[130:131], v125 offset:0x200
	ds_read_b64_tr_b16 v[132:133], v125 offset:0x600
	ds_read_b64_tr_b16 v[134:135], v125 offset:0x800
	ds_read_b64_tr_b16 v[136:137], v125 offset:0xc00
	ds_read_b64_tr_b16 v[138:139], v125 offset:0xa00
	ds_read_b64_tr_b16 v[140:141], v125 offset:0xe00
	ds_read_b128 v[144:147], v142
	ds_read_b128 v[148:151], v142 offset:512
	s_waitcnt lgkmcnt(6)
	s_nop 0
	v_mfma_f32_32x32x16_bf16 v[18:33], v[90:93], v[126:129], v[18:33]
	v_mfma_f32_32x32x16_bf16 v[2:17], v[90:93], v[130:133], v[2:17]
	ds_read_b64_tr_b16 v[126:127], v125 offset:0x1000
	ds_read_b64_tr_b16 v[128:129], v125 offset:0x1400
	ds_read_b64_tr_b16 v[130:131], v125 offset:0x1200
	ds_read_b64_tr_b16 v[132:133], v125 offset:0x1600
	ds_read_b128 v[152:155], v142 offset:2048
	ds_read_b128 v[156:159], v142 offset:2560
	s_waitcnt lgkmcnt(8)
	v_mfma_f32_32x32x16_bf16 v[18:33], v[94:97], v[134:137], v[18:33]
	v_mfma_f32_32x32x16_bf16 v[2:17], v[94:97], v[138:141], v[2:17]
	ds_read_b64_tr_b16 v[134:135], v125 offset:0x1800
	ds_read_b64_tr_b16 v[136:137], v125 offset:0x1c00
	ds_read_b64_tr_b16 v[138:139], v125 offset:0x1a00
	ds_read_b64_tr_b16 v[140:141], v125 offset:0x1e00
	ds_read_b128 v[160:163], v142 offset:4096
	ds_read_b128 v[164:167], v142 offset:4608
	s_waitcnt lgkmcnt(8)
	v_mfma_f32_32x32x16_bf16 v[18:33], v[98:101], v[126:129], v[18:33]
	s_waitcnt lgkmcnt(2)
	v_mfma_f32_32x32x16_bf16 v[2:17], v[98:101], v[130:133], v[2:17]
	v_mfma_f32_32x32x16_bf16 v[18:33], v[102:105], v[134:137], v[18:33]
	v_mfma_f32_32x32x16_bf16 v[2:17], v[102:105], v[138:141], v[2:17]
.LBB0_1049:
	s_add_i32 s14, s86, 3
	s_min_i32 s4, s14, s78
	s_ashr_i32 s5, s4, 31
	s_lshl_b64 s[12:13], s[4:5], 16
	s_and_b32 s5, s14, 3
	s_mulk_i32 s5, 0x3000
	v_lshl_add_u64 v[196:197], v[110:111], 0, s[12:13]
	s_add_i32 s12, s5, s85
	s_mov_b32 s13, m0
	s_mov_b32 m0, s12
	s_nop 0
	global_load_lds_dwordx4 v[196:197], off
	s_mov_b32 m0, s13
	s_and_b64 vcc, exec, s[8:9]
	s_cbranch_vccnz .Lmla_dma_v3
	v_mad_i64_i32 v[196:197], s[12:13], s4, v235, v[112:113]
	v_readlane_b32 s4, v254, 28
	s_add_i32 s4, s5, s4
	s_mov_b32 s5, m0
	s_mov_b32 m0, s4
	s_nop 0
	global_load_lds_dwordx4 v[196:197], off
	s_mov_b32 m0, s5
.Lmla_dma_v3:
	s_add_i32 s12, s86, 2
	s_min_i32 s12, s12, s78
	s_ashr_i32 s13, s12, 31
	s_add_i32 s15, s80, 0x6000
	s_lshl_b64 s[12:13], s[12:13], 16
	s_and_b32 s15, s15, 0x6000
	v_readlane_b32 s16, v254, 34
	s_add_i32 s15, s15, s16
	v_lshl_add_u64 v[196:197], v[114:115], 0, s[12:13]
	s_mov_b32 s12, m0
	s_mov_b32 m0, s15
	s_nop 0
	global_load_lds_dwordx4 v[196:197], off
	s_mov_b32 m0, s12
	s_cmp_ge_u32 s86, s84
	s_cselect_b64 s[4:5], -1, 0
	s_sub_i32 s12, s82, 30
	s_cmp_gt_i32 s12, s0
	s_cselect_b64 s[12:13], -1, 0
	s_or_b64 s[4:5], s[4:5], s[12:13]
	s_and_b64 vcc, exec, s[4:5]
	s_cbranch_vccnz .LBB0_1055
	ds_read_b128 v[168:171], v142 offset:6144
	ds_read_b128 v[172:175], v142 offset:6656
	ds_read_b128 v[176:179], v142 offset:8192
	ds_read_b128 v[180:183], v142 offset:8704
	ds_read_b128 v[188:191], v142 offset:10240
	ds_read_b128 v[192:195], v142 offset:10752
	s_waitcnt lgkmcnt(6)
	v_mfma_f32_32x32x16_bf16 v[50:65], v[144:147], v[66:69], 0
	v_mfma_f32_32x32x16_bf16 v[34:49], v[148:151], v[66:69], 0
	v_mfma_f32_32x32x16_bf16 v[50:65], v[152:155], v[70:73], v[50:65]
	v_mfma_f32_32x32x16_bf16 v[34:49], v[156:159], v[70:73], v[34:49]
	v_mfma_f32_32x32x16_bf16 v[50:65], v[160:163], v[74:77], v[50:65]
	v_mfma_f32_32x32x16_bf16 v[34:49], v[164:167], v[74:77], v[34:49]
	s_waitcnt lgkmcnt(4)
	v_mfma_f32_32x32x16_bf16 v[50:65], v[168:171], v[78:81], v[50:65]
	v_mfma_f32_32x32x16_bf16 v[34:49], v[172:175], v[78:81], v[34:49]
	s_waitcnt lgkmcnt(2)
	v_mfma_f32_32x32x16_bf16 v[50:65], v[176:179], v[82:85], v[50:65]
	v_mfma_f32_32x32x16_bf16 v[34:49], v[180:183], v[82:85], v[34:49]
	s_waitcnt lgkmcnt(0)
	v_mfma_f32_32x32x16_bf16 v[50:65], v[188:191], v[86:89], v[50:65]
	v_mfma_f32_32x32x16_bf16 v[34:49], v[192:195], v[86:89], v[34:49]
	s_and_b64 vcc, exec, s[6:7]
	s_mov_b64 s[4:5], -1
	s_cbranch_vccz .LBB0_1056

.LBB0_1056:
	s_waitcnt vmcnt(4) lgkmcnt(0)
	s_barrier
	s_cbranch_execz .LBB0_1052
	s_branch .LBB0_1053

.LBB0_1087:
	v_mov_b32_e32 v14, v1
	v_mov_b32_e32 v15, v1
	s_waitcnt vmcnt(0)
	v_sub_u32_e32 v16, v188, v0
	v_mov_b32_e32 v0, v1
	v_mov_b32_e32 v2, v1
	v_mov_b32_e32 v3, v1
	v_mov_b32_e32 v4, v1
	v_mov_b32_e32 v5, v1
	v_mov_b32_e32 v6, v1
	v_mov_b32_e32 v7, v1
	v_mov_b32_e32 v8, v1
	v_mov_b32_e32 v9, v1
	v_mov_b32_e32 v10, v1
	v_mov_b32_e32 v11, v1
	v_mov_b32_e32 v12, v1
	v_mov_b32_e32 v13, v1
	v_mov_b64_e32 v[64:65], v[14:15]
	v_mov_b64_e32 v[48:49], v[14:15]
	v_mov_b64_e32 v[32:33], v[14:15]
	v_cmp_lt_i32_e64 s[82:83], s79, v16
	v_mov_b64_e32 v[62:63], v[12:13]
	v_mov_b64_e32 v[60:61], v[10:11]
	v_mov_b64_e32 v[58:59], v[8:9]
	v_mov_b64_e32 v[56:57], v[6:7]
	v_mov_b64_e32 v[54:55], v[4:5]
	v_mov_b64_e32 v[52:53], v[2:3]
	v_mov_b64_e32 v[50:51], v[0:1]
	v_mov_b64_e32 v[46:47], v[12:13]
	v_mov_b64_e32 v[44:45], v[10:11]
	v_mov_b64_e32 v[42:43], v[8:9]
	v_mov_b64_e32 v[40:41], v[6:7]
	v_mov_b64_e32 v[38:39], v[4:5]
	v_mov_b64_e32 v[36:37], v[2:3]
	v_mov_b64_e32 v[34:35], v[0:1]
	v_mov_b64_e32 v[30:31], v[12:13]
	v_mov_b64_e32 v[28:29], v[10:11]
	v_mov_b64_e32 v[26:27], v[8:9]
	v_mov_b64_e32 v[24:25], v[6:7]
	v_mov_b64_e32 v[22:23], v[4:5]
	v_mov_b64_e32 v[20:21], v[2:3]
	v_mov_b64_e32 v[18:19], v[0:1]
	v_mov_b64_e32 v[16:17], v[14:15]
	s_xor_b64 s[2:3], s[12:13], -1
	s_mov_b32 s88, 0
	v_mov_b32_e32 v165, 0
	s_movk_i32 s89, 0x6000
	s_mov_b32 s78, 1
	s_mov_b32 s93, 63
	v_mov_b32_e32 v167, v198
	v_mov_b32_e32 v169, v197
	s_mov_b64 s[94:95], s[86:87]
	v_mov_b64_e32 v[14:15], v[12:13]
	v_mov_b64_e32 v[12:13], v[10:11]
	v_mov_b64_e32 v[10:11], v[8:9]
	v_mov_b64_e32 v[8:9], v[6:7]
	v_mov_b64_e32 v[6:7], v[4:5]
	v_mov_b64_e32 v[4:5], v[2:3]
	v_mov_b64_e32 v[2:3], v[0:1]
	v_mov_b32_e32 v171, 0
	s_add_i32 s4, s78, 2
	s_min_i32 s4, s4, s81
	v_mad_i64_i32 v[200:201], s[4:5], s4, v235, v[182:183]
	s_and_b32 s4, s89, 0x6000
	s_add_i32 s4, s4, s85
	s_mov_b32 s5, m0
	s_mov_b32 m0, s4
	s_nop 0
	global_load_lds_dwordx4 v[200:201], off
	s_mov_b32 m0, s5
	s_add_i32 s4, s78, 1
	s_min_i32 s5, s4, s81
	s_add_i32 s12, s88, 0x8000
	s_and_b32 s15, s12, 0xc000
	v_mad_i64_i32 v[200:201], s[12:13], s5, v235, v[150:151]
	s_add_i32 s12, s15, s75
	s_mov_b32 s13, m0
	s_mov_b32 m0, s12
	s_nop 0
	global_load_lds_dwordx4 v[200:201], off
	s_mov_b32 m0, s13
	v_mad_i64_i32 v[200:201], s[12:13], s5, v235, v[152:153]
	s_add_i32 s5, s15, s74
	s_mov_b32 s12, m0
	s_mov_b32 m0, s5
	s_nop 0
	global_load_lds_dwordx4 v[200:201], off
	s_mov_b32 m0, s12
.LBB0_1088:
	s_add_i32 s4, s78, 1
	global_load_dword v175, v1, s[94:95]
	s_sub_i32 s14, s93, 63
	s_cmp_le_i32 s14, s80
	s_cselect_b64 s[76:77], -1, 0
	s_cmp_gt_i32 s14, s80
	s_cbranch_scc1 .LBB0_1096
	v_cndmask_b32_e64 v0, 0, v195, s[82:83]
	v_sub_f32_e32 v0, v165, v0
	s_xor_b64 s[12:13], s[82:83], -1
	v_pk_add_f32 v[66:67], v[66:67], v[0:1] op_sel_hi:[1,0] neg_lo:[0,1] neg_hi:[0,1]
	v_pk_add_f32 v[82:83], v[82:83], v[0:1] op_sel_hi:[1,0] neg_lo:[0,1] neg_hi:[0,1]
	v_pk_add_f32 v[68:69], v[68:69], v[0:1] op_sel_hi:[1,0] neg_lo:[0,1] neg_hi:[0,1]
	v_pk_add_f32 v[84:85], v[84:85], v[0:1] op_sel_hi:[1,0] neg_lo:[0,1] neg_hi:[0,1]
	v_pk_add_f32 v[70:71], v[70:71], v[0:1] op_sel_hi:[1,0] neg_lo:[0,1] neg_hi:[0,1]
	v_pk_add_f32 v[86:87], v[86:87], v[0:1] op_sel_hi:[1,0] neg_lo:[0,1] neg_hi:[0,1]
	v_pk_add_f32 v[72:73], v[72:73], v[0:1] op_sel_hi:[1,0] neg_lo:[0,1] neg_hi:[0,1]
	v_pk_add_f32 v[88:89], v[88:89], v[0:1] op_sel_hi:[1,0] neg_lo:[0,1] neg_hi:[0,1]
	v_pk_add_f32 v[74:75], v[74:75], v[0:1] op_sel_hi:[1,0] neg_lo:[0,1] neg_hi:[0,1]
	v_pk_add_f32 v[90:91], v[90:91], v[0:1] op_sel_hi:[1,0] neg_lo:[0,1] neg_hi:[0,1]
	v_pk_add_f32 v[76:77], v[76:77], v[0:1] op_sel_hi:[1,0] neg_lo:[0,1] neg_hi:[0,1]
	v_pk_add_f32 v[92:93], v[92:93], v[0:1] op_sel_hi:[1,0] neg_lo:[0,1] neg_hi:[0,1]
	v_pk_add_f32 v[78:79], v[78:79], v[0:1] op_sel_hi:[1,0] neg_lo:[0,1] neg_hi:[0,1]
	v_pk_add_f32 v[94:95], v[94:95], v[0:1] op_sel_hi:[1,0] neg_lo:[0,1] neg_hi:[0,1]
	v_pk_add_f32 v[80:81], v[80:81], v[0:1] op_sel_hi:[1,0] neg_lo:[0,1] neg_hi:[0,1]
	s_andn2_b64 vcc, exec, s[12:13]
	v_pk_add_f32 v[96:97], v[96:97], v[0:1] op_sel_hi:[1,0] neg_lo:[0,1] neg_hi:[0,1]
	s_cbranch_vccnz .LBB0_1091
	v_mov_b32_e32 v0, v167
	ds_read_b128 v[114:117], v0
	ds_read_b128 v[118:121], v0 offset:128
	ds_read_b128 v[122:125], v0 offset:32
	ds_read_b128 v[126:129], v0 offset:160
	s_waitcnt lgkmcnt(3)
	v_sub_u32_e32 v114, v187, v114
	v_sub_u32_e32 v115, v187, v115
	s_waitcnt lgkmcnt(2)
	v_sub_u32_e32 v118, v187, v118
	v_med3_i32 v114, v114, 0, v241
	v_med3_i32 v115, v115, 0, v241
	v_sub_u32_e32 v119, v187, v119
	v_sub_u32_e32 v116, v187, v116
	v_sub_u32_e32 v120, v187, v120
	v_sub_u32_e32 v117, v187, v117
	v_sub_u32_e32 v121, v187, v121
	v_med3_i32 v118, v118, 0, v241
	v_lshl_add_u32 v114, v114, 2, s92
	v_med3_i32 v119, v119, 0, v241
	v_lshl_add_u32 v115, v115, 2, s92
	v_med3_i32 v116, v116, 0, v241
	v_med3_i32 v120, v120, 0, v241
	v_med3_i32 v117, v117, 0, v241
	v_med3_i32 v121, v121, 0, v241
	v_lshl_add_u32 v118, v118, 2, s92
	v_lshl_add_u32 v119, v119, 2, s92
	v_lshl_add_u32 v116, v116, 2, s92
	v_lshl_add_u32 v120, v120, 2, s92
	v_lshl_add_u32 v117, v117, 2, s92
	v_lshl_add_u32 v121, v121, 2, s92
	ds_read_b32 v200, v114
	ds_read_b32 v202, v118
	ds_read_b32 v201, v115
	ds_read_b32 v203, v119
	ds_read_b32 v204, v116
	ds_read_b32 v206, v120
	ds_read_b32 v205, v117
	ds_read_b32 v207, v121
	s_waitcnt lgkmcnt(9)
	v_sub_u32_e32 v114, v187, v122
	s_waitcnt lgkmcnt(8)
	v_sub_u32_e32 v115, v187, v126
	v_med3_i32 v114, v114, 0, v241
	v_med3_i32 v115, v115, 0, v241
	v_lshl_add_u32 v118, v114, 2, s92
	v_lshl_add_u32 v119, v115, 2, s92
	v_sub_u32_e32 v114, v187, v123
	v_sub_u32_e32 v115, v187, v127
	v_med3_i32 v114, v114, 0, v241
	v_med3_i32 v115, v115, 0, v241
	v_lshl_add_u32 v120, v114, 2, s92
	v_lshl_add_u32 v121, v115, 2, s92
	v_sub_u32_e32 v114, v187, v124
	v_sub_u32_e32 v115, v187, v128
	v_med3_i32 v114, v114, 0, v241
	v_med3_i32 v115, v115, 0, v241
	v_lshl_add_u32 v122, v114, 2, s92
	v_lshl_add_u32 v123, v115, 2, s92
	v_sub_u32_e32 v114, v187, v125
	v_sub_u32_e32 v115, v187, v129
	v_med3_i32 v114, v114, 0, v241
	v_med3_i32 v115, v115, 0, v241
	v_lshl_add_u32 v124, v114, 2, s92
	v_lshl_add_u32 v125, v115, 2, s92
	ds_read_b128 v[114:117], v0 offset:64
	ds_read_b32 v208, v118
	ds_read_b32 v210, v119
	ds_read_b32 v209, v120
	ds_read_b32 v211, v121
	ds_read_b32 v212, v122
	ds_read_b32 v214, v123
	ds_read_b32 v213, v124
	ds_read_b32 v215, v125
	ds_read_b128 v[118:121], v0 offset:192
	ds_read_b128 v[122:125], v0 offset:96
	s_waitcnt lgkmcnt(10)
	v_sub_u32_e32 v116, v187, v116
	v_med3_i32 v116, v116, 0, v241
	v_sub_u32_e32 v114, v187, v114
	ds_read_b128 v[126:129], v0 offset:224
	s_waitcnt lgkmcnt(2)
	v_sub_u32_e32 v0, v187, v118
	v_sub_u32_e32 v115, v187, v115
	v_sub_u32_e32 v118, v187, v119
	v_sub_u32_e32 v119, v187, v120
	v_lshl_add_u32 v120, v116, 2, s92
	v_sub_u32_e32 v116, v187, v117
	v_med3_i32 v114, v114, 0, v241
	v_med3_i32 v115, v115, 0, v241
	v_med3_i32 v118, v118, 0, v241
	v_med3_i32 v119, v119, 0, v241
	v_med3_i32 v116, v116, 0, v241
	v_sub_u32_e32 v117, v187, v121
	v_med3_i32 v0, v0, 0, v241
	v_lshl_add_u32 v114, v114, 2, s92
	v_lshl_add_u32 v115, v115, 2, s92
	v_lshl_add_u32 v118, v118, 2, s92
	v_lshl_add_u32 v119, v119, 2, s92
	v_med3_i32 v117, v117, 0, v241
	v_lshl_add_u32 v121, v116, 2, s92
	v_lshl_add_u32 v0, v0, 2, s92
	v_lshl_add_u32 v173, v117, 2, s92
	ds_read_b32 v114, v114
	ds_read_b32 v116, v0
	ds_read_b32 v115, v115
	ds_read_b32 v117, v118
	ds_read_b32 v118, v120
	ds_read_b32 v120, v119
	ds_read_b32 v119, v121
	ds_read_b32 v121, v173
	s_waitcnt lgkmcnt(9)
	v_sub_u32_e32 v0, v187, v122
	s_waitcnt lgkmcnt(8)
	v_sub_u32_e32 v122, v187, v126
	v_sub_u32_e32 v123, v187, v123
	v_sub_u32_e32 v126, v187, v127
	v_sub_u32_e32 v124, v187, v124
	v_sub_u32_e32 v127, v187, v128
	v_sub_u32_e32 v125, v187, v125
	v_sub_u32_e32 v128, v187, v129
	v_med3_i32 v0, v0, 0, v241
	v_med3_i32 v122, v122, 0, v241
	v_med3_i32 v123, v123, 0, v241
	v_med3_i32 v124, v124, 0, v241
	v_med3_i32 v125, v125, 0, v241
	v_med3_i32 v128, v128, 0, v241
	v_lshl_add_u32 v0, v0, 2, s92
	v_lshl_add_u32 v122, v122, 2, s92
	v_med3_i32 v126, v126, 0, v241
	v_lshl_add_u32 v123, v123, 2, s92
	v_med3_i32 v127, v127, 0, v241
	v_lshl_add_u32 v124, v124, 2, s92
	v_lshl_add_u32 v125, v125, 2, s92
	s_waitcnt lgkmcnt(1)
	v_pk_add_f32 v[76:77], v[76:77], v[118:119]
	v_lshl_add_u32 v119, v128, 2, s92
	v_lshl_add_u32 v126, v126, 2, s92
	v_lshl_add_u32 v127, v127, 2, s92
	v_pk_add_f32 v[74:75], v[74:75], v[114:115]
	ds_read_b32 v114, v0
	ds_read_b32 v118, v122
	ds_read_b32 v115, v123
	ds_read_b32 v122, v124
	ds_read_b32 v123, v125
	ds_read_b32 v125, v119
	ds_read_b32 v124, v127
	ds_read_b32 v119, v126
	v_pk_add_f32 v[66:67], v[66:67], v[200:201]
	v_pk_add_f32 v[68:69], v[68:69], v[204:205]
	v_pk_add_f32 v[70:71], v[70:71], v[208:209]
	v_pk_add_f32 v[72:73], v[72:73], v[212:213]
	s_waitcnt lgkmcnt(5)
	v_pk_add_f32 v[78:79], v[78:79], v[114:115]
	s_waitcnt lgkmcnt(3)
	v_pk_add_f32 v[80:81], v[80:81], v[122:123]
	v_pk_add_f32 v[82:83], v[82:83], v[202:203]
	v_pk_add_f32 v[84:85], v[84:85], v[206:207]
	v_pk_add_f32 v[86:87], v[86:87], v[210:211]
	v_pk_add_f32 v[88:89], v[88:89], v[214:215]
	v_pk_add_f32 v[90:91], v[90:91], v[116:117]
	v_pk_add_f32 v[92:93], v[92:93], v[120:121]
	s_waitcnt lgkmcnt(0)
	v_pk_add_f32 v[94:95], v[94:95], v[118:119]
	v_pk_add_f32 v[96:97], v[96:97], v[124:125]

.LBB0_1099:
	s_and_b32 s5, s88, 0xc000
	v_add_u32_e32 v0, s5, v196
	s_add_i32 s5, s89, 0xffffc000
	s_and_b32 s5, s5, 0x6000
	v_add_u32_e32 v177, s5, v191
	ds_read_b64_tr_b16 v[200:201], v0 offset:0
	ds_read_b64_tr_b16 v[202:203], v0 offset:0x800
	ds_read_b64_tr_b16 v[204:205], v0 offset:0x200
	ds_read_b64_tr_b16 v[206:207], v0 offset:0xa00
	ds_read_b64_tr_b16 v[208:209], v0 offset:0x400
	ds_read_b64_tr_b16 v[210:211], v0 offset:0xc00
	ds_read_b64_tr_b16 v[212:213], v0 offset:0x600
	ds_read_b64_tr_b16 v[214:215], v0 offset:0xe00
	ds_read_b64_tr_b16 v[216:217], v0 offset:0x1000
	ds_read_b64_tr_b16 v[218:219], v0 offset:0x1800
	ds_read_b64_tr_b16 v[244:245], v0 offset:0x1200
	ds_read_b64_tr_b16 v[246:247], v0 offset:0x1a00
	ds_read_b64_tr_b16 v[248:249], v0 offset:0x1400
	ds_read_b64_tr_b16 v[250:251], v0 offset:0x1c00
	ds_read_b64_tr_b16 v[228:229], v0 offset:0x1600
	ds_read_b64_tr_b16 v[230:231], v0 offset:0x1e00
	s_waitcnt lgkmcnt(8)
	s_nop 0
	v_mfma_f32_32x32x16_bf16 v[50:65], v[114:117], v[200:203], v[50:65]
	v_mfma_f32_32x32x16_bf16 v[34:49], v[114:117], v[204:207], v[34:49]
	v_mfma_f32_32x32x16_bf16 v[18:33], v[114:117], v[208:211], v[18:33]
	v_mfma_f32_32x32x16_bf16 v[2:17], v[114:117], v[212:215], v[2:17]
	ds_read_b64_tr_b16 v[200:201], v0 offset:0x2000
	ds_read_b64_tr_b16 v[202:203], v0 offset:0x2800
	ds_read_b64_tr_b16 v[204:205], v0 offset:0x2200
	ds_read_b64_tr_b16 v[206:207], v0 offset:0x2a00
	ds_read_b64_tr_b16 v[208:209], v0 offset:0x2400
	ds_read_b64_tr_b16 v[210:211], v0 offset:0x2c00
	ds_read_b64_tr_b16 v[212:213], v0 offset:0x2600
	ds_read_b64_tr_b16 v[214:215], v0 offset:0x2e00
	s_waitcnt lgkmcnt(8)
	v_mfma_f32_32x32x16_bf16 v[50:65], v[118:121], v[216:219], v[50:65]
	v_mfma_f32_32x32x16_bf16 v[34:49], v[118:121], v[244:247], v[34:49]
	v_mfma_f32_32x32x16_bf16 v[18:33], v[118:121], v[248:251], v[18:33]
	v_mfma_f32_32x32x16_bf16 v[2:17], v[118:121], v[228:231], v[2:17]
	ds_read_b64_tr_b16 v[216:217], v0 offset:0x3000
	ds_read_b64_tr_b16 v[218:219], v0 offset:0x3800
	ds_read_b64_tr_b16 v[228:229], v0 offset:0x3200
	ds_read_b64_tr_b16 v[230:231], v0 offset:0x3a00
	ds_read_b64_tr_b16 v[244:245], v0 offset:0x3400
	ds_read_b64_tr_b16 v[246:247], v0 offset:0x3c00
	ds_read_b64_tr_b16 v[248:249], v0 offset:0x3600
	ds_read_b64_tr_b16 v[250:251], v0 offset:0x3e00
	s_waitcnt lgkmcnt(8)
	v_mfma_f32_32x32x16_bf16 v[50:65], v[122:125], v[200:203], v[50:65]
	s_waitcnt lgkmcnt(0)
	v_mfma_f32_32x32x16_bf16 v[34:49], v[122:125], v[204:207], v[34:49]
	v_mfma_f32_32x32x16_bf16 v[18:33], v[122:125], v[208:211], v[18:33]
	v_mfma_f32_32x32x16_bf16 v[2:17], v[122:125], v[212:215], v[2:17]
	ds_read_b128 v[200:203], v177
	ds_read_b128 v[204:207], v177 offset:512
	ds_read_b128 v[208:211], v177 offset:2048
	ds_read_b128 v[212:215], v177 offset:2560
	v_mfma_f32_32x32x16_bf16 v[50:65], v[126:129], v[216:219], v[50:65]
	v_mfma_f32_32x32x16_bf16 v[34:49], v[126:129], v[228:231], v[34:49]
	v_mfma_f32_32x32x16_bf16 v[18:33], v[126:129], v[244:247], v[18:33]
	v_mfma_f32_32x32x16_bf16 v[2:17], v[126:129], v[248:251], v[2:17]
	ds_read_b128 v[216:219], v177 offset:4096
	ds_read_b128 v[228:231], v177 offset:4608
	ds_read_b128 v[244:247], v177 offset:6144
	ds_read_b128 v[248:251], v177 offset:6656
.LBB0_1100:
	s_add_i32 s5, s78, 3
	s_min_i32 s5, s5, s81
	v_mad_i64_i32 v[96:97], s[12:13], s5, v235, v[182:183]
	s_add_i32 s5, s89, 0x2000
	s_and_b32 s5, s5, 0x6000
	s_add_i32 s5, s5, s85
	s_mov_b32 s12, m0
	s_mov_b32 m0, s5
	s_nop 0
	global_load_lds_dwordx4 v[96:97], off
	s_mov_b32 m0, s12
	s_add_i32 s5, s78, 2
	s_min_i32 s5, s5, s81
	s_add_i32 s12, s88, 0xc000
	s_and_b32 s15, s12, 0xc000
	v_mad_i64_i32 v[96:97], s[12:13], s5, v235, v[150:151]
	s_add_i32 s12, s15, s75
	s_mov_b32 s13, m0
	s_mov_b32 m0, s12
	s_nop 0
	global_load_lds_dwordx4 v[96:97], off
	s_mov_b32 m0, s13
	v_mad_i64_i32 v[96:97], s[12:13], s5, v235, v[152:153]
	s_add_i32 s5, s15, s74
	s_mov_b32 s12, m0
	s_mov_b32 m0, s5
	s_nop 0
	global_load_lds_dwordx4 v[96:97], off
	s_mov_b32 m0, s12
	s_cmp_ge_u32 s78, s84
	s_cselect_b64 s[12:13], -1, 0
	s_sub_i32 s5, s93, 30
	s_cmp_gt_i32 s5, s0
	s_cselect_b64 s[14:15], -1, 0
	s_or_b64 s[12:13], s[12:13], s[14:15]
	s_and_b64 vcc, exec, s[12:13]
	s_cbranch_vccnz .LBB0_1106
	s_waitcnt vmcnt(3)
	v_sub_u32_e32 v0, v188, v175
	s_waitcnt lgkmcnt(7)
	v_mfma_f32_32x32x16_bf16 v[66:81], v[200:203], v[98:101], 0
	v_cmp_lt_i32_e64 s[82:83], s79, v0
	s_waitcnt lgkmcnt(6)
	v_mfma_f32_32x32x16_bf16 v[82:97], v[204:207], v[98:101], 0
	s_waitcnt lgkmcnt(5)
	v_mfma_f32_32x32x16_bf16 v[66:81], v[208:211], v[102:105], v[66:81]
	s_waitcnt lgkmcnt(4)
	v_mfma_f32_32x32x16_bf16 v[82:97], v[212:215], v[102:105], v[82:97]
	s_waitcnt lgkmcnt(3)
	v_mfma_f32_32x32x16_bf16 v[66:81], v[216:219], v[106:109], v[66:81]
	s_waitcnt lgkmcnt(2)
	v_mfma_f32_32x32x16_bf16 v[82:97], v[228:231], v[106:109], v[82:97]
	s_waitcnt lgkmcnt(1)
	v_mfma_f32_32x32x16_bf16 v[66:81], v[244:247], v[110:113], v[66:81]
	s_waitcnt lgkmcnt(0)
	v_mfma_f32_32x32x16_bf16 v[82:97], v[248:251], v[110:113], v[82:97]
	s_and_b64 vcc, exec, s[6:7]
	s_mov_b64 s[12:13], -1
	s_cbranch_vccz .LBB0_1107
